# plus chunk-A GLA gate pre-activation loop unrolled with row loads prefetched 4 rows ahead
# speedup vs baseline: 1.0106x; 1.0001x over previous
.LBB0_611:
	s_mov_b64 s[70:71], 0x1000
	v_lshl_add_u64 v[184:185], v[10:11], 0, s[70:71]
	global_load_dwordx4 v[22:25], v[10:11], off offset:-56
	global_load_dwordx4 v[26:29], v[10:11], off offset:-40
	global_load_dwordx4 v[64:67], v[10:11], off offset:-24
	global_load_dwordx4 v[68:71], v[10:11], off offset:-8
	global_load_dwordx4 v[204:207], v[10:11], off offset:456
	global_load_dwordx4 v[208:211], v[10:11], off offset:472
	global_load_dwordx4 v[212:215], v[10:11], off offset:488
	global_load_dwordx4 v[216:219], v[10:11], off offset:504
	global_load_dwordx4 v[220:223], v[10:11], off offset:968
	global_load_dwordx4 v[224:227], v[10:11], off offset:984
	global_load_dwordx4 v[228:231], v[10:11], off offset:1000
	global_load_dwordx4 v[232:235], v[10:11], off offset:1016
	global_load_dwordx4 v[176:179], v[10:11], off offset:1480
	global_load_dwordx4 v[180:183], v[10:11], off offset:1496
	global_load_dwordx4 v[244:247], v[10:11], off offset:1512
	global_load_dwordx4 v[248:251], v[10:11], off offset:1528
	s_waitcnt vmcnt(12)
	v_fma_f32 v21, v12, v22, v18
	v_fmac_f32_e32 v21, v13, v23
	v_fmac_f32_e32 v21, v14, v24
	v_fmac_f32_e32 v21, v15, v25
	v_fmac_f32_e32 v21, v16, v26
	v_pk_mul_f32 v[30:31], v[0:1], v[28:29]
	v_fmac_f32_e32 v21, v17, v27
	v_add_f32_e32 v21, v21, v30
	v_pk_mul_f32 v[48:49], v[2:3], v[64:65]
	v_add_f32_e32 v21, v21, v31
	v_add_f32_e32 v21, v21, v48
	v_pk_mul_f32 v[236:237], v[4:5], v[66:67]
	v_add_f32_e32 v21, v21, v49
	v_add_f32_e32 v21, v21, v236
	v_pk_mul_f32 v[238:239], v[6:7], v[68:69]
	v_add_f32_e32 v21, v21, v237
	v_add_f32_e32 v21, v21, v238
	v_pk_mul_f32 v[188:189], v[8:9], v[70:71]
	v_add_f32_e32 v21, v21, v239
	v_add_f32_e32 v21, v21, v188
	v_add_f32_e32 v21, v21, v189
	v_min_f32_e32 v240, 0, v21
	v_mul_f32_e64 v21, |v21|, s60
	v_exp_f32_e32 v21, v21
	s_nop 0
	v_add_f32_e32 v21, 1.0, v21
	v_cmp_gt_f32_e32 vcc, s61, v21
	s_nop 1
	v_cndmask_b32_e64 v242, 0, 32, vcc
	v_ldexp_f32 v21, v21, v242
	v_log_f32_e32 v21, v21
	v_cndmask_b32_e32 v242, 0, v199, vcc
	v_mul_f32_e32 v243, 0x3f317217, v21
	v_fma_f32 v243, v21, s62, -v243
	v_fmac_f32_e32 v243, 0x3377d1cf, v21
	v_fmac_f32_e32 v243, 0x3f317217, v21
	v_cmp_lt_f32_e64 vcc, |v21|, s36
	s_nop 1
	v_cndmask_b32_e32 v21, v21, v243, vcc
	v_sub_f32_e32 v21, v21, v242
	v_sub_f32_e32 v21, v240, v21
	v_mul_f32_e32 v21, 0x3d800000, v21
	ds_write_b32 v19, v21
	v_add_u32_e32 v19, 0x200, v19
	global_load_dwordx4 v[22:25], v[10:11], off offset:1992
	global_load_dwordx4 v[26:29], v[10:11], off offset:2008
	global_load_dwordx4 v[64:67], v[10:11], off offset:2024
	global_load_dwordx4 v[68:71], v[10:11], off offset:2040
	s_waitcnt vmcnt(12)
	v_fma_f32 v21, v12, v204, v18
	v_fmac_f32_e32 v21, v13, v205
	v_fmac_f32_e32 v21, v14, v206
	v_fmac_f32_e32 v21, v15, v207
	v_fmac_f32_e32 v21, v16, v208
	v_pk_mul_f32 v[30:31], v[0:1], v[210:211]
	v_fmac_f32_e32 v21, v17, v209
	v_add_f32_e32 v21, v21, v30
	v_pk_mul_f32 v[48:49], v[2:3], v[212:213]
	v_add_f32_e32 v21, v21, v31
	v_add_f32_e32 v21, v21, v48
	v_pk_mul_f32 v[236:237], v[4:5], v[214:215]
	v_add_f32_e32 v21, v21, v49
	v_add_f32_e32 v21, v21, v236
	v_pk_mul_f32 v[238:239], v[6:7], v[216:217]
	v_add_f32_e32 v21, v21, v237
	v_add_f32_e32 v21, v21, v238
	v_pk_mul_f32 v[188:189], v[8:9], v[218:219]
	v_add_f32_e32 v21, v21, v239
	v_add_f32_e32 v21, v21, v188
	v_add_f32_e32 v21, v21, v189
	v_min_f32_e32 v240, 0, v21
	v_mul_f32_e64 v21, |v21|, s60
	v_exp_f32_e32 v21, v21
	s_nop 0
	v_add_f32_e32 v21, 1.0, v21
	v_cmp_gt_f32_e32 vcc, s61, v21
	s_nop 1
	v_cndmask_b32_e64 v242, 0, 32, vcc
	v_ldexp_f32 v21, v21, v242
	v_log_f32_e32 v21, v21
	v_cndmask_b32_e32 v242, 0, v199, vcc
	v_mul_f32_e32 v243, 0x3f317217, v21
	v_fma_f32 v243, v21, s62, -v243
	v_fmac_f32_e32 v243, 0x3377d1cf, v21
	v_fmac_f32_e32 v243, 0x3f317217, v21
	v_cmp_lt_f32_e64 vcc, |v21|, s36
	s_nop 1
	v_cndmask_b32_e32 v21, v21, v243, vcc
	v_sub_f32_e32 v21, v21, v242
	v_sub_f32_e32 v21, v240, v21
	v_mul_f32_e32 v21, 0x3d800000, v21
	ds_write_b32 v19, v21
	v_add_u32_e32 v19, 0x200, v19
	global_load_dwordx4 v[204:207], v[10:11], off offset:2504
	global_load_dwordx4 v[208:211], v[10:11], off offset:2520
	global_load_dwordx4 v[212:215], v[10:11], off offset:2536
	global_load_dwordx4 v[216:219], v[10:11], off offset:2552
	s_waitcnt vmcnt(12)
	v_fma_f32 v21, v12, v220, v18
	v_fmac_f32_e32 v21, v13, v221
	v_fmac_f32_e32 v21, v14, v222
	v_fmac_f32_e32 v21, v15, v223
	v_fmac_f32_e32 v21, v16, v224
	v_pk_mul_f32 v[30:31], v[0:1], v[226:227]
	v_fmac_f32_e32 v21, v17, v225
	v_add_f32_e32 v21, v21, v30
	v_pk_mul_f32 v[48:49], v[2:3], v[228:229]
	v_add_f32_e32 v21, v21, v31
	v_add_f32_e32 v21, v21, v48
	v_pk_mul_f32 v[236:237], v[4:5], v[230:231]
	v_add_f32_e32 v21, v21, v49
	v_add_f32_e32 v21, v21, v236
	v_pk_mul_f32 v[238:239], v[6:7], v[232:233]
	v_add_f32_e32 v21, v21, v237
	v_add_f32_e32 v21, v21, v238
	v_pk_mul_f32 v[188:189], v[8:9], v[234:235]
	v_add_f32_e32 v21, v21, v239
	v_add_f32_e32 v21, v21, v188
	v_add_f32_e32 v21, v21, v189
	v_min_f32_e32 v240, 0, v21
	v_mul_f32_e64 v21, |v21|, s60
	v_exp_f32_e32 v21, v21
	s_nop 0
	v_add_f32_e32 v21, 1.0, v21
	v_cmp_gt_f32_e32 vcc, s61, v21
	s_nop 1
	v_cndmask_b32_e64 v242, 0, 32, vcc
	v_ldexp_f32 v21, v21, v242
	v_log_f32_e32 v21, v21
	v_cndmask_b32_e32 v242, 0, v199, vcc
	v_mul_f32_e32 v243, 0x3f317217, v21
	v_fma_f32 v243, v21, s62, -v243
	v_fmac_f32_e32 v243, 0x3377d1cf, v21
	v_fmac_f32_e32 v243, 0x3f317217, v21
	v_cmp_lt_f32_e64 vcc, |v21|, s36
	s_nop 1
	v_cndmask_b32_e32 v21, v21, v243, vcc
	v_sub_f32_e32 v21, v21, v242
	v_sub_f32_e32 v21, v240, v21
	v_mul_f32_e32 v21, 0x3d800000, v21
	ds_write_b32 v19, v21
	v_add_u32_e32 v19, 0x200, v19
	global_load_dwordx4 v[220:223], v[10:11], off offset:3016
	global_load_dwordx4 v[224:227], v[10:11], off offset:3032
	global_load_dwordx4 v[228:231], v[10:11], off offset:3048
	global_load_dwordx4 v[232:235], v[10:11], off offset:3064
	s_waitcnt vmcnt(12)
	v_fma_f32 v21, v12, v176, v18
	v_fmac_f32_e32 v21, v13, v177
	v_fmac_f32_e32 v21, v14, v178
	v_fmac_f32_e32 v21, v15, v179
	v_fmac_f32_e32 v21, v16, v180
	v_pk_mul_f32 v[30:31], v[0:1], v[182:183]
	v_fmac_f32_e32 v21, v17, v181
	v_add_f32_e32 v21, v21, v30
	v_pk_mul_f32 v[48:49], v[2:3], v[244:245]
	v_add_f32_e32 v21, v21, v31
	v_add_f32_e32 v21, v21, v48
	v_pk_mul_f32 v[236:237], v[4:5], v[246:247]
	v_add_f32_e32 v21, v21, v49
	v_add_f32_e32 v21, v21, v236
	v_pk_mul_f32 v[238:239], v[6:7], v[248:249]
	v_add_f32_e32 v21, v21, v237
	v_add_f32_e32 v21, v21, v238
	v_pk_mul_f32 v[188:189], v[8:9], v[250:251]
	v_add_f32_e32 v21, v21, v239
	v_add_f32_e32 v21, v21, v188
	v_add_f32_e32 v21, v21, v189
	v_min_f32_e32 v240, 0, v21
	v_mul_f32_e64 v21, |v21|, s60
	v_exp_f32_e32 v21, v21
	s_nop 0
	v_add_f32_e32 v21, 1.0, v21
	v_cmp_gt_f32_e32 vcc, s61, v21
	s_nop 1
	v_cndmask_b32_e64 v242, 0, 32, vcc
	v_ldexp_f32 v21, v21, v242
	v_log_f32_e32 v21, v21
	v_cndmask_b32_e32 v242, 0, v199, vcc
	v_mul_f32_e32 v243, 0x3f317217, v21
	v_fma_f32 v243, v21, s62, -v243
	v_fmac_f32_e32 v243, 0x3377d1cf, v21
	v_fmac_f32_e32 v243, 0x3f317217, v21
	v_cmp_lt_f32_e64 vcc, |v21|, s36
	s_nop 1
	v_cndmask_b32_e32 v21, v21, v243, vcc
	v_sub_f32_e32 v21, v21, v242
	v_sub_f32_e32 v21, v240, v21
	v_mul_f32_e32 v21, 0x3d800000, v21
	ds_write_b32 v19, v21
	v_add_u32_e32 v19, 0x200, v19
	global_load_dwordx4 v[176:179], v[10:11], off offset:3528
	global_load_dwordx4 v[180:183], v[10:11], off offset:3544
	global_load_dwordx4 v[244:247], v[10:11], off offset:3560
	global_load_dwordx4 v[248:251], v[10:11], off offset:3576
	s_waitcnt vmcnt(12)
	v_fma_f32 v21, v12, v22, v18
	v_fmac_f32_e32 v21, v13, v23
	v_fmac_f32_e32 v21, v14, v24
	v_fmac_f32_e32 v21, v15, v25
	v_fmac_f32_e32 v21, v16, v26
	v_pk_mul_f32 v[30:31], v[0:1], v[28:29]
	v_fmac_f32_e32 v21, v17, v27
	v_add_f32_e32 v21, v21, v30
	v_pk_mul_f32 v[48:49], v[2:3], v[64:65]
	v_add_f32_e32 v21, v21, v31
	v_add_f32_e32 v21, v21, v48
	v_pk_mul_f32 v[236:237], v[4:5], v[66:67]
	v_add_f32_e32 v21, v21, v49
	v_add_f32_e32 v21, v21, v236
	v_pk_mul_f32 v[238:239], v[6:7], v[68:69]
	v_add_f32_e32 v21, v21, v237
	v_add_f32_e32 v21, v21, v238
	v_pk_mul_f32 v[188:189], v[8:9], v[70:71]
	v_add_f32_e32 v21, v21, v239
	v_add_f32_e32 v21, v21, v188
	v_add_f32_e32 v21, v21, v189
	v_min_f32_e32 v240, 0, v21
	v_mul_f32_e64 v21, |v21|, s60
	v_exp_f32_e32 v21, v21
	s_nop 0
	v_add_f32_e32 v21, 1.0, v21
	v_cmp_gt_f32_e32 vcc, s61, v21
	s_nop 1
	v_cndmask_b32_e64 v242, 0, 32, vcc
	v_ldexp_f32 v21, v21, v242
	v_log_f32_e32 v21, v21
	v_cndmask_b32_e32 v242, 0, v199, vcc
	v_mul_f32_e32 v243, 0x3f317217, v21
	v_fma_f32 v243, v21, s62, -v243
	v_fmac_f32_e32 v243, 0x3377d1cf, v21
	v_fmac_f32_e32 v243, 0x3f317217, v21
	v_cmp_lt_f32_e64 vcc, |v21|, s36
	s_nop 1
	v_cndmask_b32_e32 v21, v21, v243, vcc
	v_sub_f32_e32 v21, v21, v242
	v_sub_f32_e32 v21, v240, v21
	v_mul_f32_e32 v21, 0x3d800000, v21
	ds_write_b32 v19, v21
	v_add_u32_e32 v19, 0x200, v19
	global_load_dwordx4 v[22:25], v[184:185], off offset:-56
	global_load_dwordx4 v[26:29], v[184:185], off offset:-40
	global_load_dwordx4 v[64:67], v[184:185], off offset:-24
	global_load_dwordx4 v[68:71], v[184:185], off offset:-8
	s_waitcnt vmcnt(12)
	v_fma_f32 v21, v12, v204, v18
	v_fmac_f32_e32 v21, v13, v205
	v_fmac_f32_e32 v21, v14, v206
	v_fmac_f32_e32 v21, v15, v207
	v_fmac_f32_e32 v21, v16, v208
	v_pk_mul_f32 v[30:31], v[0:1], v[210:211]
	v_fmac_f32_e32 v21, v17, v209
	v_add_f32_e32 v21, v21, v30
	v_pk_mul_f32 v[48:49], v[2:3], v[212:213]
	v_add_f32_e32 v21, v21, v31
	v_add_f32_e32 v21, v21, v48
	v_pk_mul_f32 v[236:237], v[4:5], v[214:215]
	v_add_f32_e32 v21, v21, v49
	v_add_f32_e32 v21, v21, v236
	v_pk_mul_f32 v[238:239], v[6:7], v[216:217]
	v_add_f32_e32 v21, v21, v237
	v_add_f32_e32 v21, v21, v238
	v_pk_mul_f32 v[188:189], v[8:9], v[218:219]
	v_add_f32_e32 v21, v21, v239
	v_add_f32_e32 v21, v21, v188
	v_add_f32_e32 v21, v21, v189
	v_min_f32_e32 v240, 0, v21
	v_mul_f32_e64 v21, |v21|, s60
	v_exp_f32_e32 v21, v21
	s_nop 0
	v_add_f32_e32 v21, 1.0, v21
	v_cmp_gt_f32_e32 vcc, s61, v21
	s_nop 1
	v_cndmask_b32_e64 v242, 0, 32, vcc
	v_ldexp_f32 v21, v21, v242
	v_log_f32_e32 v21, v21
	v_cndmask_b32_e32 v242, 0, v199, vcc
	v_mul_f32_e32 v243, 0x3f317217, v21
	v_fma_f32 v243, v21, s62, -v243
	v_fmac_f32_e32 v243, 0x3377d1cf, v21
	v_fmac_f32_e32 v243, 0x3f317217, v21
	v_cmp_lt_f32_e64 vcc, |v21|, s36
	s_nop 1
	v_cndmask_b32_e32 v21, v21, v243, vcc
	v_sub_f32_e32 v21, v21, v242
	v_sub_f32_e32 v21, v240, v21
	v_mul_f32_e32 v21, 0x3d800000, v21
	ds_write_b32 v19, v21
	v_add_u32_e32 v19, 0x200, v19
	global_load_dwordx4 v[204:207], v[184:185], off offset:456
	global_load_dwordx4 v[208:211], v[184:185], off offset:472
	global_load_dwordx4 v[212:215], v[184:185], off offset:488
	global_load_dwordx4 v[216:219], v[184:185], off offset:504
	s_waitcnt vmcnt(12)
	v_fma_f32 v21, v12, v220, v18
	v_fmac_f32_e32 v21, v13, v221
	v_fmac_f32_e32 v21, v14, v222
	v_fmac_f32_e32 v21, v15, v223
	v_fmac_f32_e32 v21, v16, v224
	v_pk_mul_f32 v[30:31], v[0:1], v[226:227]
	v_fmac_f32_e32 v21, v17, v225
	v_add_f32_e32 v21, v21, v30
	v_pk_mul_f32 v[48:49], v[2:3], v[228:229]
	v_add_f32_e32 v21, v21, v31
	v_add_f32_e32 v21, v21, v48
	v_pk_mul_f32 v[236:237], v[4:5], v[230:231]
	v_add_f32_e32 v21, v21, v49
	v_add_f32_e32 v21, v21, v236
	v_pk_mul_f32 v[238:239], v[6:7], v[232:233]
	v_add_f32_e32 v21, v21, v237
	v_add_f32_e32 v21, v21, v238
	v_pk_mul_f32 v[188:189], v[8:9], v[234:235]
	v_add_f32_e32 v21, v21, v239
	v_add_f32_e32 v21, v21, v188
	v_add_f32_e32 v21, v21, v189
	v_min_f32_e32 v240, 0, v21
	v_mul_f32_e64 v21, |v21|, s60
	v_exp_f32_e32 v21, v21
	s_nop 0
	v_add_f32_e32 v21, 1.0, v21
	v_cmp_gt_f32_e32 vcc, s61, v21
	s_nop 1
	v_cndmask_b32_e64 v242, 0, 32, vcc
	v_ldexp_f32 v21, v21, v242
	v_log_f32_e32 v21, v21
	v_cndmask_b32_e32 v242, 0, v199, vcc
	v_mul_f32_e32 v243, 0x3f317217, v21
	v_fma_f32 v243, v21, s62, -v243
	v_fmac_f32_e32 v243, 0x3377d1cf, v21
	v_fmac_f32_e32 v243, 0x3f317217, v21
	v_cmp_lt_f32_e64 vcc, |v21|, s36
	s_nop 1
	v_cndmask_b32_e32 v21, v21, v243, vcc
	v_sub_f32_e32 v21, v21, v242
	v_sub_f32_e32 v21, v240, v21
	v_mul_f32_e32 v21, 0x3d800000, v21
	ds_write_b32 v19, v21
	v_add_u32_e32 v19, 0x200, v19
	global_load_dwordx4 v[220:223], v[184:185], off offset:968
	global_load_dwordx4 v[224:227], v[184:185], off offset:984
	global_load_dwordx4 v[228:231], v[184:185], off offset:1000
	global_load_dwordx4 v[232:235], v[184:185], off offset:1016
	s_waitcnt vmcnt(12)
	v_fma_f32 v21, v12, v176, v18
	v_fmac_f32_e32 v21, v13, v177
	v_fmac_f32_e32 v21, v14, v178
	v_fmac_f32_e32 v21, v15, v179
	v_fmac_f32_e32 v21, v16, v180
	v_pk_mul_f32 v[30:31], v[0:1], v[182:183]
	v_fmac_f32_e32 v21, v17, v181
	v_add_f32_e32 v21, v21, v30
	v_pk_mul_f32 v[48:49], v[2:3], v[244:245]
	v_add_f32_e32 v21, v21, v31
	v_add_f32_e32 v21, v21, v48
	v_pk_mul_f32 v[236:237], v[4:5], v[246:247]
	v_add_f32_e32 v21, v21, v49
	v_add_f32_e32 v21, v21, v236
	v_pk_mul_f32 v[238:239], v[6:7], v[248:249]
	v_add_f32_e32 v21, v21, v237
	v_add_f32_e32 v21, v21, v238
	v_pk_mul_f32 v[188:189], v[8:9], v[250:251]
	v_add_f32_e32 v21, v21, v239
	v_add_f32_e32 v21, v21, v188
	v_add_f32_e32 v21, v21, v189
	v_min_f32_e32 v240, 0, v21
	v_mul_f32_e64 v21, |v21|, s60
	v_exp_f32_e32 v21, v21
	s_nop 0
	v_add_f32_e32 v21, 1.0, v21
	v_cmp_gt_f32_e32 vcc, s61, v21
	s_nop 1
	v_cndmask_b32_e64 v242, 0, 32, vcc
	v_ldexp_f32 v21, v21, v242
	v_log_f32_e32 v21, v21
	v_cndmask_b32_e32 v242, 0, v199, vcc
	v_mul_f32_e32 v243, 0x3f317217, v21
	v_fma_f32 v243, v21, s62, -v243
	v_fmac_f32_e32 v243, 0x3377d1cf, v21
	v_fmac_f32_e32 v243, 0x3f317217, v21
	v_cmp_lt_f32_e64 vcc, |v21|, s36
	s_nop 1
	v_cndmask_b32_e32 v21, v21, v243, vcc
	v_sub_f32_e32 v21, v21, v242
	v_sub_f32_e32 v21, v240, v21
	v_mul_f32_e32 v21, 0x3d800000, v21
	ds_write_b32 v19, v21
	v_add_u32_e32 v19, 0x200, v19
	global_load_dwordx4 v[176:179], v[184:185], off offset:1480
	global_load_dwordx4 v[180:183], v[184:185], off offset:1496
	global_load_dwordx4 v[244:247], v[184:185], off offset:1512
	global_load_dwordx4 v[248:251], v[184:185], off offset:1528
	s_waitcnt vmcnt(12)
	v_fma_f32 v21, v12, v22, v18
	v_fmac_f32_e32 v21, v13, v23
	v_fmac_f32_e32 v21, v14, v24
	v_fmac_f32_e32 v21, v15, v25
	v_fmac_f32_e32 v21, v16, v26
	v_pk_mul_f32 v[30:31], v[0:1], v[28:29]
	v_fmac_f32_e32 v21, v17, v27
	v_add_f32_e32 v21, v21, v30
	v_pk_mul_f32 v[48:49], v[2:3], v[64:65]
	v_add_f32_e32 v21, v21, v31
	v_add_f32_e32 v21, v21, v48
	v_pk_mul_f32 v[236:237], v[4:5], v[66:67]
	v_add_f32_e32 v21, v21, v49
	v_add_f32_e32 v21, v21, v236
	v_pk_mul_f32 v[238:239], v[6:7], v[68:69]
	v_add_f32_e32 v21, v21, v237
	v_add_f32_e32 v21, v21, v238
	v_pk_mul_f32 v[188:189], v[8:9], v[70:71]
	v_add_f32_e32 v21, v21, v239
	v_add_f32_e32 v21, v21, v188
	v_add_f32_e32 v21, v21, v189
	v_min_f32_e32 v240, 0, v21
	v_mul_f32_e64 v21, |v21|, s60
	v_exp_f32_e32 v21, v21
	s_nop 0
	v_add_f32_e32 v21, 1.0, v21
	v_cmp_gt_f32_e32 vcc, s61, v21
	s_nop 1
	v_cndmask_b32_e64 v242, 0, 32, vcc
	v_ldexp_f32 v21, v21, v242
	v_log_f32_e32 v21, v21
	v_cndmask_b32_e32 v242, 0, v199, vcc
	v_mul_f32_e32 v243, 0x3f317217, v21
	v_fma_f32 v243, v21, s62, -v243
	v_fmac_f32_e32 v243, 0x3377d1cf, v21
	v_fmac_f32_e32 v243, 0x3f317217, v21
	v_cmp_lt_f32_e64 vcc, |v21|, s36
	s_nop 1
	v_cndmask_b32_e32 v21, v21, v243, vcc
	v_sub_f32_e32 v21, v21, v242
	v_sub_f32_e32 v21, v240, v21
	v_mul_f32_e32 v21, 0x3d800000, v21
	ds_write_b32 v19, v21
	v_add_u32_e32 v19, 0x200, v19
	global_load_dwordx4 v[22:25], v[184:185], off offset:1992
	global_load_dwordx4 v[26:29], v[184:185], off offset:2008
	global_load_dwordx4 v[64:67], v[184:185], off offset:2024
	global_load_dwordx4 v[68:71], v[184:185], off offset:2040
	s_waitcnt vmcnt(12)
	v_fma_f32 v21, v12, v204, v18
	v_fmac_f32_e32 v21, v13, v205
	v_fmac_f32_e32 v21, v14, v206
	v_fmac_f32_e32 v21, v15, v207
	v_fmac_f32_e32 v21, v16, v208
	v_pk_mul_f32 v[30:31], v[0:1], v[210:211]
	v_fmac_f32_e32 v21, v17, v209
	v_add_f32_e32 v21, v21, v30
	v_pk_mul_f32 v[48:49], v[2:3], v[212:213]
	v_add_f32_e32 v21, v21, v31
	v_add_f32_e32 v21, v21, v48
	v_pk_mul_f32 v[236:237], v[4:5], v[214:215]
	v_add_f32_e32 v21, v21, v49
	v_add_f32_e32 v21, v21, v236
	v_pk_mul_f32 v[238:239], v[6:7], v[216:217]
	v_add_f32_e32 v21, v21, v237
	v_add_f32_e32 v21, v21, v238
	v_pk_mul_f32 v[188:189], v[8:9], v[218:219]
	v_add_f32_e32 v21, v21, v239
	v_add_f32_e32 v21, v21, v188
	v_add_f32_e32 v21, v21, v189
	v_min_f32_e32 v240, 0, v21
	v_mul_f32_e64 v21, |v21|, s60
	v_exp_f32_e32 v21, v21
	s_nop 0
	v_add_f32_e32 v21, 1.0, v21
	v_cmp_gt_f32_e32 vcc, s61, v21
	s_nop 1
	v_cndmask_b32_e64 v242, 0, 32, vcc
	v_ldexp_f32 v21, v21, v242
	v_log_f32_e32 v21, v21
	v_cndmask_b32_e32 v242, 0, v199, vcc
	v_mul_f32_e32 v243, 0x3f317217, v21
	v_fma_f32 v243, v21, s62, -v243
	v_fmac_f32_e32 v243, 0x3377d1cf, v21
	v_fmac_f32_e32 v243, 0x3f317217, v21
	v_cmp_lt_f32_e64 vcc, |v21|, s36
	s_nop 1
	v_cndmask_b32_e32 v21, v21, v243, vcc
	v_sub_f32_e32 v21, v21, v242
	v_sub_f32_e32 v21, v240, v21
	v_mul_f32_e32 v21, 0x3d800000, v21
	ds_write_b32 v19, v21
	v_add_u32_e32 v19, 0x200, v19
	global_load_dwordx4 v[204:207], v[184:185], off offset:2504
	global_load_dwordx4 v[208:211], v[184:185], off offset:2520
	global_load_dwordx4 v[212:215], v[184:185], off offset:2536
	global_load_dwordx4 v[216:219], v[184:185], off offset:2552
	s_waitcnt vmcnt(12)
	v_fma_f32 v21, v12, v220, v18
	v_fmac_f32_e32 v21, v13, v221
	v_fmac_f32_e32 v21, v14, v222
	v_fmac_f32_e32 v21, v15, v223
	v_fmac_f32_e32 v21, v16, v224
	v_pk_mul_f32 v[30:31], v[0:1], v[226:227]
	v_fmac_f32_e32 v21, v17, v225
	v_add_f32_e32 v21, v21, v30
	v_pk_mul_f32 v[48:49], v[2:3], v[228:229]
	v_add_f32_e32 v21, v21, v31
	v_add_f32_e32 v21, v21, v48
	v_pk_mul_f32 v[236:237], v[4:5], v[230:231]
	v_add_f32_e32 v21, v21, v49
	v_add_f32_e32 v21, v21, v236
	v_pk_mul_f32 v[238:239], v[6:7], v[232:233]
	v_add_f32_e32 v21, v21, v237
	v_add_f32_e32 v21, v21, v238
	v_pk_mul_f32 v[188:189], v[8:9], v[234:235]
	v_add_f32_e32 v21, v21, v239
	v_add_f32_e32 v21, v21, v188
	v_add_f32_e32 v21, v21, v189
	v_min_f32_e32 v240, 0, v21
	v_mul_f32_e64 v21, |v21|, s60
	v_exp_f32_e32 v21, v21
	s_nop 0
	v_add_f32_e32 v21, 1.0, v21
	v_cmp_gt_f32_e32 vcc, s61, v21
	s_nop 1
	v_cndmask_b32_e64 v242, 0, 32, vcc
	v_ldexp_f32 v21, v21, v242
	v_log_f32_e32 v21, v21
	v_cndmask_b32_e32 v242, 0, v199, vcc
	v_mul_f32_e32 v243, 0x3f317217, v21
	v_fma_f32 v243, v21, s62, -v243
	v_fmac_f32_e32 v243, 0x3377d1cf, v21
	v_fmac_f32_e32 v243, 0x3f317217, v21
	v_cmp_lt_f32_e64 vcc, |v21|, s36
	s_nop 1
	v_cndmask_b32_e32 v21, v21, v243, vcc
	v_sub_f32_e32 v21, v21, v242
	v_sub_f32_e32 v21, v240, v21
	v_mul_f32_e32 v21, 0x3d800000, v21
	ds_write_b32 v19, v21
	v_add_u32_e32 v19, 0x200, v19
	global_load_dwordx4 v[220:223], v[184:185], off offset:3016
	global_load_dwordx4 v[224:227], v[184:185], off offset:3032
	global_load_dwordx4 v[228:231], v[184:185], off offset:3048
	global_load_dwordx4 v[232:235], v[184:185], off offset:3064
	s_waitcnt vmcnt(12)
	v_fma_f32 v21, v12, v176, v18
	v_fmac_f32_e32 v21, v13, v177
	v_fmac_f32_e32 v21, v14, v178
	v_fmac_f32_e32 v21, v15, v179
	v_fmac_f32_e32 v21, v16, v180
	v_pk_mul_f32 v[30:31], v[0:1], v[182:183]
	v_fmac_f32_e32 v21, v17, v181
	v_add_f32_e32 v21, v21, v30
	v_pk_mul_f32 v[48:49], v[2:3], v[244:245]
	v_add_f32_e32 v21, v21, v31
	v_add_f32_e32 v21, v21, v48
	v_pk_mul_f32 v[236:237], v[4:5], v[246:247]
	v_add_f32_e32 v21, v21, v49
	v_add_f32_e32 v21, v21, v236
	v_pk_mul_f32 v[238:239], v[6:7], v[248:249]
	v_add_f32_e32 v21, v21, v237
	v_add_f32_e32 v21, v21, v238
	v_pk_mul_f32 v[188:189], v[8:9], v[250:251]
	v_add_f32_e32 v21, v21, v239
	v_add_f32_e32 v21, v21, v188
	v_add_f32_e32 v21, v21, v189
	v_min_f32_e32 v240, 0, v21
	v_mul_f32_e64 v21, |v21|, s60
	v_exp_f32_e32 v21, v21
	s_nop 0
	v_add_f32_e32 v21, 1.0, v21
	v_cmp_gt_f32_e32 vcc, s61, v21
	s_nop 1
	v_cndmask_b32_e64 v242, 0, 32, vcc
	v_ldexp_f32 v21, v21, v242
	v_log_f32_e32 v21, v21
	v_cndmask_b32_e32 v242, 0, v199, vcc
	v_mul_f32_e32 v243, 0x3f317217, v21
	v_fma_f32 v243, v21, s62, -v243
	v_fmac_f32_e32 v243, 0x3377d1cf, v21
	v_fmac_f32_e32 v243, 0x3f317217, v21
	v_cmp_lt_f32_e64 vcc, |v21|, s36
	s_nop 1
	v_cndmask_b32_e32 v21, v21, v243, vcc
	v_sub_f32_e32 v21, v21, v242
	v_sub_f32_e32 v21, v240, v21
	v_mul_f32_e32 v21, 0x3d800000, v21
	ds_write_b32 v19, v21
	v_add_u32_e32 v19, 0x200, v19
	global_load_dwordx4 v[176:179], v[184:185], off offset:3528
	global_load_dwordx4 v[180:183], v[184:185], off offset:3544
	global_load_dwordx4 v[244:247], v[184:185], off offset:3560
	global_load_dwordx4 v[248:251], v[184:185], off offset:3576
	s_waitcnt vmcnt(12)
	v_fma_f32 v21, v12, v22, v18
	v_fmac_f32_e32 v21, v13, v23
	v_fmac_f32_e32 v21, v14, v24
	v_fmac_f32_e32 v21, v15, v25
	v_fmac_f32_e32 v21, v16, v26
	v_pk_mul_f32 v[30:31], v[0:1], v[28:29]
	v_fmac_f32_e32 v21, v17, v27
	v_add_f32_e32 v21, v21, v30
	v_pk_mul_f32 v[48:49], v[2:3], v[64:65]
	v_add_f32_e32 v21, v21, v31
	v_add_f32_e32 v21, v21, v48
	v_pk_mul_f32 v[236:237], v[4:5], v[66:67]
	v_add_f32_e32 v21, v21, v49
	v_add_f32_e32 v21, v21, v236
	v_pk_mul_f32 v[238:239], v[6:7], v[68:69]
	v_add_f32_e32 v21, v21, v237
	v_add_f32_e32 v21, v21, v238
	v_pk_mul_f32 v[188:189], v[8:9], v[70:71]
	v_add_f32_e32 v21, v21, v239
	v_add_f32_e32 v21, v21, v188
	v_add_f32_e32 v21, v21, v189
	v_min_f32_e32 v240, 0, v21
	v_mul_f32_e64 v21, |v21|, s60
	v_exp_f32_e32 v21, v21
	s_nop 0
	v_add_f32_e32 v21, 1.0, v21
	v_cmp_gt_f32_e32 vcc, s61, v21
	s_nop 1
	v_cndmask_b32_e64 v242, 0, 32, vcc
	v_ldexp_f32 v21, v21, v242
	v_log_f32_e32 v21, v21
	v_cndmask_b32_e32 v242, 0, v199, vcc
	v_mul_f32_e32 v243, 0x3f317217, v21
	v_fma_f32 v243, v21, s62, -v243
	v_fmac_f32_e32 v243, 0x3377d1cf, v21
	v_fmac_f32_e32 v243, 0x3f317217, v21
	v_cmp_lt_f32_e64 vcc, |v21|, s36
	s_nop 1
	v_cndmask_b32_e32 v21, v21, v243, vcc
	v_sub_f32_e32 v21, v21, v242
	v_sub_f32_e32 v21, v240, v21
	v_mul_f32_e32 v21, 0x3d800000, v21
	ds_write_b32 v19, v21
	v_add_u32_e32 v19, 0x200, v19
	s_waitcnt vmcnt(8)
	v_fma_f32 v21, v12, v204, v18
	v_fmac_f32_e32 v21, v13, v205
	v_fmac_f32_e32 v21, v14, v206
	v_fmac_f32_e32 v21, v15, v207
	v_fmac_f32_e32 v21, v16, v208
	v_pk_mul_f32 v[30:31], v[0:1], v[210:211]
	v_fmac_f32_e32 v21, v17, v209
	v_add_f32_e32 v21, v21, v30
	v_pk_mul_f32 v[48:49], v[2:3], v[212:213]
	v_add_f32_e32 v21, v21, v31
	v_add_f32_e32 v21, v21, v48
	v_pk_mul_f32 v[236:237], v[4:5], v[214:215]
	v_add_f32_e32 v21, v21, v49
	v_add_f32_e32 v21, v21, v236
	v_pk_mul_f32 v[238:239], v[6:7], v[216:217]
	v_add_f32_e32 v21, v21, v237
	v_add_f32_e32 v21, v21, v238
	v_pk_mul_f32 v[188:189], v[8:9], v[218:219]
	v_add_f32_e32 v21, v21, v239
	v_add_f32_e32 v21, v21, v188
	v_add_f32_e32 v21, v21, v189
	v_min_f32_e32 v240, 0, v21
	v_mul_f32_e64 v21, |v21|, s60
	v_exp_f32_e32 v21, v21
	s_nop 0
	v_add_f32_e32 v21, 1.0, v21
	v_cmp_gt_f32_e32 vcc, s61, v21
	s_nop 1
	v_cndmask_b32_e64 v242, 0, 32, vcc
	v_ldexp_f32 v21, v21, v242
	v_log_f32_e32 v21, v21
	v_cndmask_b32_e32 v242, 0, v199, vcc
	v_mul_f32_e32 v243, 0x3f317217, v21
	v_fma_f32 v243, v21, s62, -v243
	v_fmac_f32_e32 v243, 0x3377d1cf, v21
	v_fmac_f32_e32 v243, 0x3f317217, v21
	v_cmp_lt_f32_e64 vcc, |v21|, s36
	s_nop 1
	v_cndmask_b32_e32 v21, v21, v243, vcc
	v_sub_f32_e32 v21, v21, v242
	v_sub_f32_e32 v21, v240, v21
	v_mul_f32_e32 v21, 0x3d800000, v21
	ds_write_b32 v19, v21
	v_add_u32_e32 v19, 0x200, v19
	s_waitcnt vmcnt(4)
	v_fma_f32 v21, v12, v220, v18
	v_fmac_f32_e32 v21, v13, v221
	v_fmac_f32_e32 v21, v14, v222
	v_fmac_f32_e32 v21, v15, v223
	v_fmac_f32_e32 v21, v16, v224
	v_pk_mul_f32 v[30:31], v[0:1], v[226:227]
	v_fmac_f32_e32 v21, v17, v225
	v_add_f32_e32 v21, v21, v30
	v_pk_mul_f32 v[48:49], v[2:3], v[228:229]
	v_add_f32_e32 v21, v21, v31
	v_add_f32_e32 v21, v21, v48
	v_pk_mul_f32 v[236:237], v[4:5], v[230:231]
	v_add_f32_e32 v21, v21, v49
	v_add_f32_e32 v21, v21, v236
	v_pk_mul_f32 v[238:239], v[6:7], v[232:233]
	v_add_f32_e32 v21, v21, v237
	v_add_f32_e32 v21, v21, v238
	v_pk_mul_f32 v[188:189], v[8:9], v[234:235]
	v_add_f32_e32 v21, v21, v239
	v_add_f32_e32 v21, v21, v188
	v_add_f32_e32 v21, v21, v189
	v_min_f32_e32 v240, 0, v21
	v_mul_f32_e64 v21, |v21|, s60
	v_exp_f32_e32 v21, v21
	s_nop 0
	v_add_f32_e32 v21, 1.0, v21
	v_cmp_gt_f32_e32 vcc, s61, v21
	s_nop 1
	v_cndmask_b32_e64 v242, 0, 32, vcc
	v_ldexp_f32 v21, v21, v242
	v_log_f32_e32 v21, v21
	v_cndmask_b32_e32 v242, 0, v199, vcc
	v_mul_f32_e32 v243, 0x3f317217, v21
	v_fma_f32 v243, v21, s62, -v243
	v_fmac_f32_e32 v243, 0x3377d1cf, v21
	v_fmac_f32_e32 v243, 0x3f317217, v21
	v_cmp_lt_f32_e64 vcc, |v21|, s36
	s_nop 1
	v_cndmask_b32_e32 v21, v21, v243, vcc
	v_sub_f32_e32 v21, v21, v242
	v_sub_f32_e32 v21, v240, v21
	v_mul_f32_e32 v21, 0x3d800000, v21
	ds_write_b32 v19, v21
	v_add_u32_e32 v19, 0x200, v19
	s_waitcnt vmcnt(0)
	v_fma_f32 v21, v12, v176, v18
	v_fmac_f32_e32 v21, v13, v177
	v_fmac_f32_e32 v21, v14, v178
	v_fmac_f32_e32 v21, v15, v179
	v_fmac_f32_e32 v21, v16, v180
	v_pk_mul_f32 v[30:31], v[0:1], v[182:183]
	v_fmac_f32_e32 v21, v17, v181
	v_add_f32_e32 v21, v21, v30
	v_pk_mul_f32 v[48:49], v[2:3], v[244:245]
	v_add_f32_e32 v21, v21, v31
	v_add_f32_e32 v21, v21, v48
	v_pk_mul_f32 v[236:237], v[4:5], v[246:247]
	v_add_f32_e32 v21, v21, v49
	v_add_f32_e32 v21, v21, v236
	v_pk_mul_f32 v[238:239], v[6:7], v[248:249]
	v_add_f32_e32 v21, v21, v237
	v_add_f32_e32 v21, v21, v238
	v_pk_mul_f32 v[188:189], v[8:9], v[250:251]
	v_add_f32_e32 v21, v21, v239
	v_add_f32_e32 v21, v21, v188
	v_add_f32_e32 v21, v21, v189
	v_min_f32_e32 v240, 0, v21
	v_mul_f32_e64 v21, |v21|, s60
	v_exp_f32_e32 v21, v21
	s_nop 0
	v_add_f32_e32 v21, 1.0, v21
	v_cmp_gt_f32_e32 vcc, s61, v21
	s_nop 1
	v_cndmask_b32_e64 v242, 0, 32, vcc
	v_ldexp_f32 v21, v21, v242
	v_log_f32_e32 v21, v21
	v_cndmask_b32_e32 v242, 0, v199, vcc
	v_mul_f32_e32 v243, 0x3f317217, v21
	v_fma_f32 v243, v21, s62, -v243
	v_fmac_f32_e32 v243, 0x3377d1cf, v21
	v_fmac_f32_e32 v243, 0x3f317217, v21
	v_cmp_lt_f32_e64 vcc, |v21|, s36
	s_nop 1
	v_cndmask_b32_e32 v21, v21, v243, vcc
	v_sub_f32_e32 v21, v21, v242
	v_sub_f32_e32 v21, v240, v21
	v_mul_f32_e32 v21, 0x3d800000, v21
	ds_write_b32 v19, v21
	v_add_u32_e32 v19, 0x200, v19
	s_mov_b32 s36, 0x7f800000
	s_or_b64 exec, exec, s[58:59]
	s_waitcnt lgkmcnt(0)
	s_barrier
	s_and_saveexec_b64 s[58:59], s[38:39]
	s_cbranch_execz .LBB0_616
	s_add_i32 s21, s93, s21
	s_and_b32 s21, s21, 7
	s_lshl_b32 s21, s21, 7
	s_add_i32 s60, s21, 0xfffffe00
	s_mov_b32 s61, s5
	s_ashr_i32 s67, s66, 31
	s_lshl_b64 s[60:61], s[60:61], 2
	s_lshl_b64 s[62:63], s[66:67], 11
	s_add_u32 s60, s62, s60
	s_addc_u32 s61, s63, s61
	v_lshl_add_u64 v[0:1], v[44:45], 0, s[60:61]
	v_mov_b32_e32 v3, 0
	s_mov_b64 s[60:61], 0
	v_mov_b32_e32 v2, v58
